# MoBA phase A gate loop: natural-order q registers (no per-iteration shuffles), one address add, DPP exchange, branch-free top-3 insertion
# speedup vs baseline: 1.0069x; 1.0069x over previous
; __global__ void __launch_bounds__(NWAVES * 64, 2) mk_fwd(Args args) {
;     ...
;                         const int row = ftid >> 1, half = ftid & 1;
;                         float q[64];
;                         { const bf16_t* qp = W_qb + ((size_t)h_ * T + qb_ * 256 + row) * 128 + half * 64;
; #pragma unroll
;                           for (int i = 0; i < 8; ++i) { const bf16x8 v = *(const bf16x8*)(qp + i * 8);
; #pragma unroll
;                               for (int jj = 0; jj < 8; ++jj) q[i * 8 + jj] = bf2f((unsigned short)v[jj]); } }
;                         float v0 = -INFINITY, v1 = -INFINITY, v2 = -INFINITY; int i0 = -1, i1 = -1, i2 = -1;
; #pragma unroll 1
;                         for (int n = 0; n < qb_; ++n) {
.LBB0_568:
	s_or_b64 exec, exec, s[10:11]
	s_lshl_b32 s64, s35, 8
	v_lshl_add_u64 v[8:9], v[6:7], 0, s[64:65]
	v_lshlrev_b64 v[10:11], 8, v[8:9]
	v_lshl_add_u64 v[10:11], v[2:3], 0, v[10:11]
	s_waitcnt lgkmcnt(0)
	s_barrier
	global_load_dwordx4 v[92:95], v[10:11], off
	global_load_dwordx4 v[96:99], v[10:11], off offset:16
	global_load_dwordx4 v[100:103], v[10:11], off offset:32
	global_load_dwordx4 v[104:107], v[10:11], off offset:48
	global_load_dwordx4 v[108:111], v[10:11], off offset:64
	global_load_dwordx4 v[112:115], v[10:11], off offset:80
	global_load_dwordx4 v[116:119], v[10:11], off offset:96
	global_load_dwordx4 v[120:123], v[10:11], off offset:112
	s_xor_b64 s[10:11], s[12:13], -1
	s_waitcnt vmcnt(7)
	v_lshlrev_b32_e32 v10, 16, v92
	v_and_b32_e32 v11, 0xffff0000, v92
	v_lshlrev_b32_e32 v12, 16, v93
	v_and_b32_e32 v13, 0xffff0000, v93
	v_lshlrev_b32_e32 v14, 16, v94
	v_and_b32_e32 v15, 0xffff0000, v94
	v_lshlrev_b32_e32 v16, 16, v95
	v_and_b32_e32 v17, 0xffff0000, v95
	s_waitcnt vmcnt(6)
	v_lshlrev_b32_e32 v18, 16, v96
	v_and_b32_e32 v19, 0xffff0000, v96
	v_lshlrev_b32_e32 v20, 16, v97
	v_and_b32_e32 v21, 0xffff0000, v97
	v_lshlrev_b32_e32 v22, 16, v98
	v_and_b32_e32 v23, 0xffff0000, v98
	v_lshlrev_b32_e32 v24, 16, v99
	v_and_b32_e32 v25, 0xffff0000, v99
	s_waitcnt vmcnt(5)
	v_lshlrev_b32_e32 v26, 16, v100
	v_and_b32_e32 v27, 0xffff0000, v100
	v_lshlrev_b32_e32 v28, 16, v101
	v_and_b32_e32 v29, 0xffff0000, v101
	v_lshlrev_b32_e32 v30, 16, v102
	v_and_b32_e32 v31, 0xffff0000, v102
	v_lshlrev_b32_e32 v32, 16, v103
	v_and_b32_e32 v33, 0xffff0000, v103
	s_waitcnt vmcnt(4)
	v_lshlrev_b32_e32 v34, 16, v104
	v_and_b32_e32 v35, 0xffff0000, v104
	v_lshlrev_b32_e32 v36, 16, v105
	v_and_b32_e32 v37, 0xffff0000, v105
	v_lshlrev_b32_e32 v38, 16, v106
	v_and_b32_e32 v39, 0xffff0000, v106
	v_lshlrev_b32_e32 v40, 16, v107
	v_and_b32_e32 v41, 0xffff0000, v107
	s_waitcnt vmcnt(3)
	v_lshlrev_b32_e32 v42, 16, v108
	v_and_b32_e32 v43, 0xffff0000, v108
	v_lshlrev_b32_e32 v44, 16, v109
	v_and_b32_e32 v45, 0xffff0000, v109
	v_lshlrev_b32_e32 v46, 16, v110
	v_and_b32_e32 v47, 0xffff0000, v110
	v_lshlrev_b32_e32 v48, 16, v111
	v_and_b32_e32 v49, 0xffff0000, v111
	s_waitcnt vmcnt(2)
	v_lshlrev_b32_e32 v50, 16, v112
	v_and_b32_e32 v51, 0xffff0000, v112
	v_lshlrev_b32_e32 v52, 16, v113
	v_and_b32_e32 v53, 0xffff0000, v113
	v_lshlrev_b32_e32 v54, 16, v114
	v_and_b32_e32 v55, 0xffff0000, v114
	v_lshlrev_b32_e32 v56, 16, v115
	v_and_b32_e32 v57, 0xffff0000, v115
	s_waitcnt vmcnt(1)
	v_lshlrev_b32_e32 v58, 16, v116
	v_and_b32_e32 v59, 0xffff0000, v116
	v_lshlrev_b32_e32 v60, 16, v117
	v_and_b32_e32 v61, 0xffff0000, v117
	v_lshlrev_b32_e32 v62, 16, v118
	v_and_b32_e32 v63, 0xffff0000, v118
	v_lshlrev_b32_e32 v64, 16, v119
	v_and_b32_e32 v65, 0xffff0000, v119
	s_waitcnt vmcnt(0)
	v_lshlrev_b32_e32 v66, 16, v120
	v_and_b32_e32 v67, 0xffff0000, v120
	v_lshlrev_b32_e32 v68, 16, v121
	v_and_b32_e32 v69, 0xffff0000, v121
	v_lshlrev_b32_e32 v70, 16, v122
	v_and_b32_e32 v71, 0xffff0000, v122
	v_lshlrev_b32_e32 v72, 16, v123
	v_and_b32_e32 v73, 0xffff0000, v123
	v_mov_b32_e32 v85, -1
	v_mov_b32_e32 v84, -1
	v_mov_b32_e32 v83, -1
	v_mov_b32_e32 v124, 0xff800000
	v_mov_b32_e32 v125, 0xff800000
	v_mov_b32_e32 v126, 0xff800000
	v_add_u32_e32 v88, 0x10800, v80
	s_mov_b32 s36, 0
	s_mov_b32 s37, 0
	s_cmp_eq_u32 s35, 0
	s_cbranch_scc1 .Lpa_done
; #define LAS __attribute__((address_space(3)))
; __global__ void __launch_bounds__(NWAVES * 64, 2) mk_fwd(Args args) {
;     ...
;                         for (int n = 0; n < qb_; ++n) {
;                             const LAS float* kp = km + n * 136 + half * 68;
;                             float a0 = 0.f, a1 = 0.f, a2 = 0.f, a3 = 0.f;
; #pragma unroll
;                             for (int jj = 0; jj < 64; jj += 4) { const f32x4 kv = *(const LAS f32x4*)(kp + jj);
;                                 a0 += q[jj] * kv[0]; a1 += q[jj + 1] * kv[1]; a2 += q[jj + 2] * kv[2]; a3 += q[jj + 3] * kv[3]; }
;                             float gsc = (a0 + a1) + (a2 + a3); gsc += __shfl_xor(gsc, 1);
;                             if (gsc > v0) { v2 = v1; i2 = i1; v1 = v0; i1 = i0; v0 = gsc; i0 = n; }
;                             else if (gsc > v1) { v2 = v1; i2 = i1; v1 = gsc; i1 = n; }
;                             else if (gsc > v2) { v2 = gsc; i2 = n; }
;                         }
;                         {
;                             float l1 = 0.f;
; #pragma unroll
;                             for (int i = 0; i < 64; ++i) l1 += fabsf(q[i]);
;                             l1 += __shfl_xor(l1, 1);
;                             const float kmaxv = __uint_as_float(__hip_atomic_load(W_ctl + 12288 + j * 64 + h_, __ATOMIC_RELAXED, __HIP_MEMORY_SCOPE_AGENT));
;                             const float Bq = mb::SCALE * l1 * kmaxv * 1.02f, slope = exp2f(-(float)(h_ + 1) * 0.5f);
;                             const float Dz = (2.f * Bq + 104.f) / slope, posf = (float)(qb_ * 256 + row - 255);
;                             if (i0 >= 0 && posf - (float)(i0 * 256) > Dz) i0 = -1;
;                             if (i1 >= 0 && posf - (float)(i1 * 256) > Dz) i1 = -1;
;                             if (i2 >= 0 && posf - (float)(i2 * 256) > Dz) i2 = -1;
.Lpa_loop:
	v_add_u32_e32 v127, s36, v88
	ds_read_b128 v[92:95], v127
	ds_read_b128 v[96:99], v127 offset:16
	ds_read_b128 v[100:103], v127 offset:32
	ds_read_b128 v[104:107], v127 offset:48
	ds_read_b128 v[108:111], v127 offset:64
	ds_read_b128 v[112:115], v127 offset:80
	ds_read_b128 v[116:119], v127 offset:96
	ds_read_b128 v[120:123], v127 offset:112
	s_waitcnt lgkmcnt(7)
	v_pk_fma_f32 v[130:131], v[10:11], v[92:93], 0 op_sel_hi:[1,1,0]
	v_pk_fma_f32 v[132:133], v[12:13], v[94:95], 0 op_sel_hi:[1,1,0]
	ds_read_b128 v[92:95], v127 offset:128
	s_waitcnt lgkmcnt(7)
	v_pk_fma_f32 v[130:131], v[14:15], v[96:97], v[130:131]
	v_pk_fma_f32 v[132:133], v[16:17], v[98:99], v[132:133]
	ds_read_b128 v[96:99], v127 offset:144
	s_waitcnt lgkmcnt(7)
	v_pk_fma_f32 v[130:131], v[18:19], v[100:101], v[130:131]
	v_pk_fma_f32 v[132:133], v[20:21], v[102:103], v[132:133]
	ds_read_b128 v[100:103], v127 offset:160
	s_waitcnt lgkmcnt(7)
	v_pk_fma_f32 v[130:131], v[22:23], v[104:105], v[130:131]
	v_pk_fma_f32 v[132:133], v[24:25], v[106:107], v[132:133]
	ds_read_b128 v[104:107], v127 offset:176
	s_waitcnt lgkmcnt(7)
	v_pk_fma_f32 v[130:131], v[26:27], v[108:109], v[130:131]
	v_pk_fma_f32 v[132:133], v[28:29], v[110:111], v[132:133]
	ds_read_b128 v[108:111], v127 offset:192
	s_waitcnt lgkmcnt(7)
	v_pk_fma_f32 v[130:131], v[30:31], v[112:113], v[130:131]
	v_pk_fma_f32 v[132:133], v[32:33], v[114:115], v[132:133]
	ds_read_b128 v[112:115], v127 offset:208
	s_waitcnt lgkmcnt(7)
	v_pk_fma_f32 v[130:131], v[34:35], v[116:117], v[130:131]
	v_pk_fma_f32 v[132:133], v[36:37], v[118:119], v[132:133]
	ds_read_b128 v[116:119], v127 offset:224
	s_waitcnt lgkmcnt(7)
	v_pk_fma_f32 v[130:131], v[38:39], v[120:121], v[130:131]
	v_pk_fma_f32 v[132:133], v[40:41], v[122:123], v[132:133]
	ds_read_b128 v[120:123], v127 offset:240
	s_waitcnt lgkmcnt(7)
	v_pk_fma_f32 v[130:131], v[42:43], v[92:93], v[130:131]
	v_pk_fma_f32 v[132:133], v[44:45], v[94:95], v[132:133]
	s_waitcnt lgkmcnt(6)
	v_pk_fma_f32 v[130:131], v[46:47], v[96:97], v[130:131]
	v_pk_fma_f32 v[132:133], v[48:49], v[98:99], v[132:133]
	s_waitcnt lgkmcnt(5)
	v_pk_fma_f32 v[130:131], v[50:51], v[100:101], v[130:131]
	v_pk_fma_f32 v[132:133], v[52:53], v[102:103], v[132:133]
	s_waitcnt lgkmcnt(4)
	v_pk_fma_f32 v[130:131], v[54:55], v[104:105], v[130:131]
	v_pk_fma_f32 v[132:133], v[56:57], v[106:107], v[132:133]
	s_waitcnt lgkmcnt(3)
	v_pk_fma_f32 v[130:131], v[58:59], v[108:109], v[130:131]
	v_pk_fma_f32 v[132:133], v[60:61], v[110:111], v[132:133]
	s_waitcnt lgkmcnt(2)
	v_pk_fma_f32 v[130:131], v[62:63], v[112:113], v[130:131]
	v_pk_fma_f32 v[132:133], v[64:65], v[114:115], v[132:133]
	s_waitcnt lgkmcnt(1)
	v_pk_fma_f32 v[130:131], v[66:67], v[116:117], v[130:131]
	v_pk_fma_f32 v[132:133], v[68:69], v[118:119], v[132:133]
	s_waitcnt lgkmcnt(0)
	v_pk_fma_f32 v[130:131], v[70:71], v[120:121], v[130:131]
	v_pk_fma_f32 v[132:133], v[72:73], v[122:123], v[132:133]
	v_add_f32_e32 v134, v130, v131
	v_add_f32_e32 v135, v132, v133
	v_mov_b32_e32 v136, s37
	v_add_f32_e32 v134, v134, v135
	s_nop 1
	v_mov_b32_dpp v135, v134 quad_perm:[1,0,3,2] row_mask:0xf bank_mask:0xf
	s_add_i32 s37, s37, 1
	s_addk_i32 s36, 0x220
	v_add_f32_e32 v134, v134, v135
	v_cmp_gt_f32_e64 s[12:13], v134, v124
	v_cmp_gt_f32_e64 s[14:15], v134, v125
	v_cmp_gt_f32_e64 s[16:17], v134, v126
	v_cndmask_b32_e64 v126, v126, v134, s[16:17]
	v_cndmask_b32_e64 v83, v83, v136, s[16:17]
	v_cndmask_b32_e64 v126, v126, v125, s[14:15]
	v_cndmask_b32_e64 v83, v83, v84, s[14:15]
	v_cndmask_b32_e64 v125, v125, v134, s[14:15]
	v_cndmask_b32_e64 v84, v84, v136, s[14:15]
	v_cndmask_b32_e64 v125, v125, v124, s[12:13]
	v_cndmask_b32_e64 v84, v84, v85, s[12:13]
	v_cndmask_b32_e64 v124, v124, v134, s[12:13]
	v_cndmask_b32_e64 v85, v85, v136, s[12:13]
	s_cmp_eq_u32 s37, s35
	s_cbranch_scc0 .Lpa_loop
.Lpa_done:
	v_add_f32_e64 v10, |v10|, |v11|
	v_add_f32_e64 v10, v10, |v12|
	v_add_f32_e64 v10, v10, |v13|
	v_add_f32_e64 v10, v10, |v14|
	v_add_f32_e64 v10, v10, |v15|
	v_add_f32_e64 v10, v10, |v16|
	v_add_f32_e64 v10, v10, |v17|
	v_add_f32_e64 v10, v10, |v18|
	v_add_f32_e64 v10, v10, |v19|
	v_add_f32_e64 v10, v10, |v20|
	v_add_f32_e64 v10, v10, |v21|
	v_add_f32_e64 v10, v10, |v22|
	v_add_f32_e64 v10, v10, |v23|
	v_add_f32_e64 v10, v10, |v24|
	v_add_f32_e64 v10, v10, |v25|
	v_add_f32_e64 v10, v10, |v26|
	v_add_f32_e64 v10, v10, |v27|
	v_add_f32_e64 v10, v10, |v28|
	v_add_f32_e64 v10, v10, |v29|
	v_add_f32_e64 v10, v10, |v30|
	v_add_f32_e64 v10, v10, |v31|
	v_add_f32_e64 v10, v10, |v32|
	v_add_f32_e64 v10, v10, |v33|
	v_add_f32_e64 v10, v10, |v34|
	v_add_f32_e64 v10, v10, |v35|
	v_add_f32_e64 v10, v10, |v36|
	v_add_f32_e64 v10, v10, |v37|
	v_add_f32_e64 v10, v10, |v38|
	v_add_f32_e64 v10, v10, |v39|
	v_add_f32_e64 v10, v10, |v40|
	v_add_f32_e64 v10, v10, |v41|
	v_add_f32_e64 v10, v10, |v42|
	v_add_f32_e64 v10, v10, |v43|
	v_add_f32_e64 v10, v10, |v44|
	v_add_f32_e64 v10, v10, |v45|
	v_add_f32_e64 v10, v10, |v46|
	v_add_f32_e64 v10, v10, |v47|
	v_add_f32_e64 v10, v10, |v48|
	v_add_f32_e64 v10, v10, |v49|
	v_add_f32_e64 v10, v10, |v50|
	v_add_f32_e64 v10, v10, |v51|
	v_add_f32_e64 v10, v10, |v52|
	v_add_f32_e64 v10, v10, |v53|
	v_add_f32_e64 v10, v10, |v54|
	v_add_f32_e64 v10, v10, |v55|
	v_add_f32_e64 v10, v10, |v56|
	v_add_f32_e64 v10, v10, |v57|
	v_add_f32_e64 v10, v10, |v58|
	v_add_f32_e64 v10, v10, |v59|
	v_add_f32_e64 v10, v10, |v60|
	v_add_f32_e64 v10, v10, |v61|
	v_add_f32_e64 v10, v10, |v62|
	v_add_f32_e64 v10, v10, |v63|
	v_add_f32_e64 v10, v10, |v64|
	v_add_f32_e64 v10, v10, |v65|
	v_add_f32_e64 v10, v10, |v66|
	v_add_f32_e64 v10, v10, |v67|
	v_add_f32_e64 v10, v10, |v68|
	v_add_f32_e64 v10, v10, |v69|
	v_add_f32_e64 v10, v10, |v70|
	v_add_f32_e64 v10, v10, |v71|
	v_add_f32_e64 v10, v10, |v72|
	v_add_f32_e64 v10, v10, |v73|
	ds_bpermute_b32 v11, v76, v10
	s_waitcnt lgkmcnt(0)
	v_add_f32_e32 v10, v10, v11
	global_load_dword v11, v129, s[8:9] sc1
	v_mul_f32_e32 v10, 0x3db504f3, v10
	s_waitcnt vmcnt(0)
	v_mul_f32_e32 v10, v10, v11
	v_mul_f32_e32 v10, 0x3f828f5c, v10
	v_fmaak_f32 v10, 2.0, v10, 0x42d00000
	v_div_scale_f32 v11, s[12:13], v82, v82, v10
	v_rcp_f32_e32 v12, v11
	s_nop 0
	v_fma_f32 v13, -v11, v12, 1.0
	v_fmac_f32_e32 v12, v13, v12
	v_div_scale_f32 v13, vcc, v10, v82, v10
	v_mul_f32_e32 v14, v13, v12
	v_fma_f32 v15, -v11, v14, v13
	v_fmac_f32_e32 v14, v15, v12
	v_fma_f32 v11, -v11, v14, v13
	v_div_fmas_f32 v11, v11, v12, v14
	v_div_fixup_f32 v10, v11, v82, v10
	v_add_u32_e32 v11, s64, v77
	v_cvt_f32_i32_e32 v11, v11
	v_cmp_lt_i32_e32 vcc, -1, v85
	s_and_saveexec_b64 s[12:13], vcc
	s_cbranch_execz .LBB0_587
	v_lshlrev_b32_e32 v12, 8, v85
	v_cvt_f32_u32_e32 v12, v12
	v_sub_f32_e32 v12, v11, v12
	v_cmp_gt_f32_e32 vcc, v12, v10
	s_and_saveexec_b64 s[14:15], vcc
	v_mov_b32_e32 v85, -1
	s_or_b64 exec, exec, s[14:15]
	s_or_b64 exec, exec, s[12:13]
	v_cmp_lt_i32_e32 vcc, -1, v84
	s_and_saveexec_b64 s[12:13], vcc
	s_cbranch_execnz .LBB0_588
